# write-through (sc1) stores for the G1/G2 GEMM outputs and the attention O tile (barrier-published tensors: less for buffer_wbl2 to flush at the seam)
# baseline (speedup 1.0000x reference)
.LBB0_520:
	s_lshl_b32 s2, s80, 8
	s_cmp_gt_i32 s53, 0
	s_cselect_b32 s3, 0x80, 0
	s_or_b32 s2, s3, s2
	v_add_u32_e32 v130, s2, v222
	v_ashrrev_i32_e32 v131, 31, v130
	v_mul_lo_u32 v132, s10, v131
	v_mul_lo_u32 v133, s11, v130
	v_mad_u64_u32 v[130:131], s[2:3], s10, v130, 0
	v_add3_u32 v131, v131, v132, v133
	s_lshl_b32 s2, s69, 8
	v_lshl_add_u64 v[130:131], v[130:131], 1, s[18:19]
	s_ashr_i32 s3, s2, 31
	v_lshl_add_u64 v[130:131], s[2:3], 1, v[130:131]
	s_mov_b32 s69, s73
	v_lshl_add_u64 v[130:131], v[130:131], 0, s[68:69]
	v_lshl_add_u64 v[130:131], v[130:131], 0, v[128:129]
	v_cvt_pk_bf16_f32 v124, v124, v125
	v_cvt_pk_bf16_f32 v125, v126, v127
	v_cvt_pk_bf16_f32 v126, v120, v121
	v_cvt_pk_bf16_f32 v127, v122, v123
	global_store_dwordx4 v[130:131], v[124:127], off sc1
	v_cvt_pk_bf16_f32 v112, v112, v113
	v_cvt_pk_bf16_f32 v113, v114, v115
	v_cvt_pk_bf16_f32 v114, v104, v105
	v_cvt_pk_bf16_f32 v115, v106, v107
	global_store_dwordx4 v[130:131], v[112:115], off offset:256 sc1
	v_cvt_pk_bf16_f32 v104, v116, v117
	v_cvt_pk_bf16_f32 v105, v118, v119
	v_cvt_pk_bf16_f32 v106, v108, v109
	v_cvt_pk_bf16_f32 v107, v110, v111
	s_cmp_gt_i32 s53, -1
	s_nop 0
	v_lshl_add_u64 v[112:113], v[130:131], 0, s[62:63]
	global_store_dwordx4 v[112:113], v[104:107], off sc1
	v_cvt_pk_bf16_f32 v96, v96, v97
	v_cvt_pk_bf16_f32 v97, v98, v99
	v_cvt_pk_bf16_f32 v98, v88, v89
	v_cvt_pk_bf16_f32 v99, v90, v91
	global_store_dwordx4 v[112:113], v[96:99], off offset:256 sc1
	v_cvt_pk_bf16_f32 v88, v100, v101
	v_cvt_pk_bf16_f32 v89, v102, v103
	v_cvt_pk_bf16_f32 v90, v92, v93
	v_cvt_pk_bf16_f32 v91, v94, v95
	s_nop 1
	v_lshl_add_u64 v[96:97], v[112:113], 0, s[62:63]
	global_store_dwordx4 v[96:97], v[88:91], off sc1
	v_cvt_pk_bf16_f32 v80, v80, v81
	v_cvt_pk_bf16_f32 v81, v82, v83
	v_cvt_pk_bf16_f32 v82, v72, v73
	v_lshl_add_u64 v[72:73], v[96:97], 0, s[62:63]
	v_cvt_pk_bf16_f32 v83, v74, v75
	global_store_dwordx4 v[96:97], v[80:83], off offset:256 sc1
	v_cvt_pk_bf16_f32 v74, v84, v85
	v_cvt_pk_bf16_f32 v75, v86, v87
	v_cvt_pk_bf16_f32 v76, v76, v77
	v_cvt_pk_bf16_f32 v77, v78, v79
	global_store_dwordx4 v[72:73], v[74:77], off sc1
	v_cvt_pk_bf16_f32 v68, v68, v69
	v_cvt_pk_bf16_f32 v69, v70, v71
	v_cvt_pk_bf16_f32 v70, v64, v65
	v_cvt_pk_bf16_f32 v71, v66, v67
	global_store_dwordx4 v[72:73], v[68:71], off offset:256 sc1
	s_cbranch_scc1 .LBB0_522
	v_lshl_add_u64 v[64:65], v[72:73], 0, s[64:65]
	v_cvt_pk_bf16_f32 v60, v60, v61
	v_cvt_pk_bf16_f32 v61, v62, v63
	v_cvt_pk_bf16_f32 v62, v56, v57
	v_cvt_pk_bf16_f32 v63, v58, v59
	global_store_dwordx4 v[64:65], v[60:63], off sc1
	v_cvt_pk_bf16_f32 v52, v52, v53
	v_cvt_pk_bf16_f32 v53, v54, v55
	v_cvt_pk_bf16_f32 v54, v48, v49
	v_lshl_add_u64 v[48:49], v[64:65], 0, s[62:63]
	v_cvt_pk_bf16_f32 v55, v50, v51
	global_store_dwordx4 v[64:65], v[52:55], off offset:256 sc1
	v_cvt_pk_bf16_f32 v44, v44, v45
	v_cvt_pk_bf16_f32 v45, v46, v47
	v_cvt_pk_bf16_f32 v46, v40, v41
	v_cvt_pk_bf16_f32 v47, v42, v43
	global_store_dwordx4 v[48:49], v[44:47], off sc1
	v_cvt_pk_bf16_f32 v36, v36, v37
	v_cvt_pk_bf16_f32 v37, v38, v39
	v_cvt_pk_bf16_f32 v38, v32, v33
	v_lshl_add_u64 v[32:33], v[48:49], 0, s[62:63]
	v_cvt_pk_bf16_f32 v39, v34, v35
	global_store_dwordx4 v[48:49], v[36:39], off offset:256 sc1
	v_cvt_pk_bf16_f32 v28, v28, v29
	v_cvt_pk_bf16_f32 v29, v30, v31
	v_cvt_pk_bf16_f32 v30, v24, v25
	v_cvt_pk_bf16_f32 v31, v26, v27
	global_store_dwordx4 v[32:33], v[28:31], off sc1
	v_cvt_pk_bf16_f32 v20, v20, v21
	v_cvt_pk_bf16_f32 v21, v22, v23
	v_cvt_pk_bf16_f32 v22, v16, v17
	v_lshl_add_u64 v[16:17], v[32:33], 0, s[62:63]
	v_cvt_pk_bf16_f32 v23, v18, v19
	global_store_dwordx4 v[32:33], v[20:23], off offset:256 sc1
	v_cvt_pk_bf16_f32 v12, v12, v13
	v_cvt_pk_bf16_f32 v13, v14, v15
	v_cvt_pk_bf16_f32 v14, v8, v9
	v_cvt_pk_bf16_f32 v15, v10, v11
	global_store_dwordx4 v[16:17], v[12:15], off sc1
	v_cvt_pk_bf16_f32 v4, v4, v5
	v_cvt_pk_bf16_f32 v5, v6, v7
	v_cvt_pk_bf16_f32 v6, v0, v1
	v_cvt_pk_bf16_f32 v7, v2, v3
	global_store_dwordx4 v[16:17], v[4:7], off offset:256 sc1

.LBB0_728:
	s_cmp_eq_u32 s81, 0
	s_mov_b32 s2, 0x32800000
	s_cselect_b32 s2, s2, 0x39400000
	s_movk_i32 s3, 0xc00
	s_cselect_b32 s15, s3, 0x1000
	s_add_u32 s2, s6, s2
	v_lshl_add_u32 v145, s80, 8, v142
	s_addc_u32 s3, s7, 0
	v_mad_i64_i32 v[146:147], s[22:23], s15, v145, 0
	v_lshl_add_u64 v[146:147], v[146:147], 1, s[2:3]
	s_lshl_b32 s2, s13, 8
	s_ashr_i32 s3, s2, 31
	v_lshl_add_u64 v[146:147], s[2:3], 1, v[146:147]
	s_mov_b32 s13, s73
	v_lshl_add_u64 v[146:147], v[146:147], 0, s[12:13]
	v_lshl_add_u64 v[146:147], v[146:147], 0, v[128:129]
	v_cvt_pk_bf16_f32 v124, v124, v125
	v_cvt_pk_bf16_f32 v125, v126, v127
	v_cvt_pk_bf16_f32 v126, v120, v121
	v_cvt_pk_bf16_f32 v127, v122, v123
	global_store_dwordx4 v[146:147], v[124:127], off sc1
	v_cvt_pk_bf16_f32 v112, v112, v113
	v_cvt_pk_bf16_f32 v113, v114, v115
	s_lshl_b32 s22, s15, 5
	s_mov_b32 s23, s73
	v_cvt_pk_bf16_f32 v114, v104, v105
	v_cvt_pk_bf16_f32 v115, v106, v107
	global_store_dwordx4 v[146:147], v[112:115], off offset:256 sc1
	v_cvt_pk_bf16_f32 v104, v116, v117
	v_cvt_pk_bf16_f32 v105, v118, v119
	v_cvt_pk_bf16_f32 v106, v108, v109
	v_cvt_pk_bf16_f32 v107, v110, v111
	s_mul_i32 s2, s15, 0xa0
	s_nop 0
	v_lshl_add_u64 v[112:113], v[146:147], 0, s[22:23]
	global_store_dwordx4 v[112:113], v[104:107], off sc1
	v_cvt_pk_bf16_f32 v96, v96, v97
	v_cvt_pk_bf16_f32 v97, v98, v99
	v_cvt_pk_bf16_f32 v98, v88, v89
	v_cvt_pk_bf16_f32 v99, v90, v91
	global_store_dwordx4 v[112:113], v[96:99], off offset:256 sc1
	v_cvt_pk_bf16_f32 v88, v100, v101
	v_cvt_pk_bf16_f32 v89, v102, v103
	v_cvt_pk_bf16_f32 v90, v92, v93
	v_cvt_pk_bf16_f32 v91, v94, v95
	s_mov_b32 s3, s73
	s_nop 0
	v_lshl_add_u64 v[96:97], v[112:113], 0, s[22:23]
	global_store_dwordx4 v[96:97], v[88:91], off sc1
	v_cvt_pk_bf16_f32 v80, v80, v81
	v_cvt_pk_bf16_f32 v81, v82, v83
	v_cvt_pk_bf16_f32 v82, v72, v73
	v_cvt_pk_bf16_f32 v83, v74, v75
	global_store_dwordx4 v[96:97], v[80:83], off offset:256 sc1
	v_cvt_pk_bf16_f32 v72, v84, v85
	v_cvt_pk_bf16_f32 v73, v86, v87
	v_cvt_pk_bf16_f32 v74, v76, v77
	v_cvt_pk_bf16_f32 v75, v78, v79
	s_andn2_b64 vcc, exec, s[58:59]
	s_nop 0
	v_lshl_add_u64 v[80:81], v[96:97], 0, s[22:23]
	global_store_dwordx4 v[80:81], v[72:75], off sc1
	v_cvt_pk_bf16_f32 v68, v68, v69
	v_cvt_pk_bf16_f32 v69, v70, v71
	v_cvt_pk_bf16_f32 v70, v64, v65
	v_lshl_add_u64 v[64:65], v[80:81], 0, s[2:3]
	v_cvt_pk_bf16_f32 v71, v66, v67
	global_store_dwordx4 v[80:81], v[68:71], off offset:256 sc1
	v_cvt_pk_bf16_f32 v60, v60, v61
	v_cvt_pk_bf16_f32 v61, v62, v63
	v_cvt_pk_bf16_f32 v62, v56, v57
	v_cvt_pk_bf16_f32 v63, v58, v59
	global_store_dwordx4 v[64:65], v[60:63], off sc1
	v_cvt_pk_bf16_f32 v48, v48, v49
	v_cvt_pk_bf16_f32 v49, v50, v51
	v_cvt_pk_bf16_f32 v50, v40, v41
	v_cvt_pk_bf16_f32 v51, v42, v43
	global_store_dwordx4 v[64:65], v[48:51], off offset:256 sc1
	v_cvt_pk_bf16_f32 v40, v52, v53
	v_cvt_pk_bf16_f32 v41, v54, v55
	v_cvt_pk_bf16_f32 v42, v44, v45
	v_cvt_pk_bf16_f32 v43, v46, v47
	s_nop 1
	v_lshl_add_u64 v[48:49], v[64:65], 0, s[22:23]
	global_store_dwordx4 v[48:49], v[40:43], off sc1
	v_cvt_pk_bf16_f32 v32, v32, v33
	v_cvt_pk_bf16_f32 v33, v34, v35
	v_cvt_pk_bf16_f32 v34, v24, v25
	v_cvt_pk_bf16_f32 v35, v26, v27
	global_store_dwordx4 v[48:49], v[32:35], off offset:256 sc1
	v_cvt_pk_bf16_f32 v24, v36, v37
	v_cvt_pk_bf16_f32 v25, v38, v39
	v_cvt_pk_bf16_f32 v26, v28, v29
	v_cvt_pk_bf16_f32 v27, v30, v31
	s_nop 1
	v_lshl_add_u64 v[32:33], v[48:49], 0, s[22:23]
	global_store_dwordx4 v[32:33], v[24:27], off sc1
	v_cvt_pk_bf16_f32 v16, v16, v17
	v_cvt_pk_bf16_f32 v17, v18, v19
	v_cvt_pk_bf16_f32 v18, v8, v9
	v_cvt_pk_bf16_f32 v19, v10, v11
	global_store_dwordx4 v[32:33], v[16:19], off offset:256 sc1
	v_cvt_pk_bf16_f32 v8, v20, v21
	v_cvt_pk_bf16_f32 v9, v22, v23
	v_cvt_pk_bf16_f32 v10, v12, v13
	v_cvt_pk_bf16_f32 v11, v14, v15
	s_nop 1
	v_lshl_add_u64 v[16:17], v[32:33], 0, s[22:23]
	s_mov_b64 s[22:23], -1
	global_store_dwordx4 v[16:17], v[8:11], off sc1
	v_cvt_pk_bf16_f32 v4, v4, v5
	v_cvt_pk_bf16_f32 v5, v6, v7
	v_cvt_pk_bf16_f32 v6, v0, v1
	v_cvt_pk_bf16_f32 v7, v2, v3
	global_store_dwordx4 v[16:17], v[4:7], off offset:256 sc1
	s_cbranch_vccnz .LBB0_721
	s_andn2_b64 vcc, exec, s[8:9]
	s_cbranch_vccnz .LBB0_720
	s_barrier
	s_branch .LBB0_720

.LBB0_799:
	v_cndmask_b32_e64 v65, v65, v206, s[58:59]
	v_mul_f32_e32 v65, 0xbe0293ee, v65
	v_fmamk_f32 v67, v113, 0x3e0293ee, v65
	v_exp_f32_e32 v83, v67
	v_fmamk_f32 v67, v112, 0x3e0293ee, v65
	v_exp_f32_e32 v85, v67
	v_fmamk_f32 v67, v111, 0x3e0293ee, v65
	v_exp_f32_e32 v81, v67
	v_fmamk_f32 v67, v110, 0x3e0293ee, v65
	v_exp_f32_e32 v87, v67
	v_fmamk_f32 v67, v109, 0x3e0293ee, v65
	v_exp_f32_e32 v89, v67
	v_fmamk_f32 v67, v108, 0x3e0293ee, v65
	v_exp_f32_e32 v91, v67
	v_fmamk_f32 v67, v107, 0x3e0293ee, v65
	v_exp_f32_e32 v93, v67
	v_fmamk_f32 v67, v106, 0x3e0293ee, v65
	v_exp_f32_e32 v95, v67
	v_fmamk_f32 v67, v105, 0x3e0293ee, v65
	v_exp_f32_e32 v105, v67
	v_fmamk_f32 v67, v104, 0x3e0293ee, v65
	v_exp_f32_e32 v107, v67
	v_fmamk_f32 v67, v103, 0x3e0293ee, v65
	v_exp_f32_e32 v77, v67
	v_fmamk_f32 v67, v102, 0x3e0293ee, v65
	v_exp_f32_e32 v103, v67
	v_fmamk_f32 v67, v99, 0x3e0293ee, v65
	v_exp_f32_e32 v99, v67
	v_fmamk_f32 v67, v98, 0x3e0293ee, v65
	v_exp_f32_e32 v109, v67
	v_fmamk_f32 v67, v97, 0x3e0293ee, v65
	v_exp_f32_e32 v75, v67
	v_fmamk_f32 v67, v96, 0x3e0293ee, v65
	v_exp_f32_e32 v97, v67
	v_fmamk_f32 v67, v79, 0x3e0293ee, v65
	v_fmamk_f32 v69, v125, 0x3e0293ee, v65
	v_fmamk_f32 v70, v124, 0x3e0293ee, v65
	v_fmamk_f32 v73, v123, 0x3e0293ee, v65
	v_fmamk_f32 v78, v122, 0x3e0293ee, v65
	v_fmamk_f32 v79, v121, 0x3e0293ee, v65
	v_fmamk_f32 v80, v120, 0x3e0293ee, v65
	v_fmamk_f32 v72, v72, 0x3e0293ee, v65
	v_fmamk_f32 v71, v71, 0x3e0293ee, v65
	v_fmamk_f32 v82, v119, 0x3e0293ee, v65
	v_fmamk_f32 v76, v118, 0x3e0293ee, v65
	v_fmamk_f32 v84, v117, 0x3e0293ee, v65
	v_fmamk_f32 v86, v116, 0x3e0293ee, v65
	v_fmamk_f32 v88, v115, 0x3e0293ee, v65
	v_fmamk_f32 v74, v114, 0x3e0293ee, v65
	v_fmac_f32_e32 v65, 0x3e0293ee, v64
	v_exp_f32_e32 v96, v65
	v_exp_f32_e32 v74, v74
	v_exp_f32_e32 v94, v72
	v_exp_f32_e32 v92, v80
	v_exp_f32_e32 v108, v88
	v_exp_f32_e32 v90, v79
	v_exp_f32_e32 v98, v86
	v_exp_f32_e32 v88, v78
	v_exp_f32_e32 v102, v84
	v_exp_f32_e32 v86, v73
	v_exp_f32_e32 v76, v76
	v_exp_f32_e32 v104, v71
	v_exp_f32_e32 v80, v70
	v_pk_add_f32 v[70:71], v[96:97], v[74:75]
	v_pk_add_f32 v[72:73], v[94:95], v[92:93]
	v_exp_f32_e32 v106, v82
	v_exp_f32_e32 v84, v69
	v_pk_add_f32 v[70:71], v[108:109], v[70:71]
	v_pk_add_f32 v[72:73], v[90:91], v[72:73]
	v_exp_f32_e32 v82, v67
	v_pk_add_f32 v[70:71], v[98:99], v[70:71]
	v_pk_add_f32 v[72:73], v[88:89], v[72:73]
	v_pk_add_f32 v[70:71], v[102:103], v[70:71]
	v_pk_add_f32 v[72:73], v[86:87], v[72:73]
	v_pk_add_f32 v[70:71], v[76:77], v[70:71]
	v_pk_add_f32 v[72:73], v[80:81], v[72:73]
	v_pk_add_f32 v[70:71], v[106:107], v[70:71]
	v_pk_add_f32 v[72:73], v[84:85], v[72:73]
	v_pk_add_f32 v[70:71], v[104:105], v[70:71]
	v_pk_add_f32 v[72:73], v[82:83], v[72:73]
	s_lshl_b64 s[2:3], s[78:79], 12
	v_pk_add_f32 v[70:71], v[72:73], v[70:71]
	s_add_u32 s6, s35, s2
	v_pk_add_f32 v[70:71], v[70:71], v[70:71] op_sel:[0,1] op_sel_hi:[1,0]
	s_addc_u32 s7, s36, s3
	s_lshl_b32 s2, s15, 7
	v_mov_b32_e32 v69, v70
	s_ashr_i32 s3, s2, 31
	s_nop 0
	v_permlane32_swap_b32_e32 v70, v69
	s_lshl_b64 s[2:3], s[2:3], 1
	v_mul_f32_e32 v64, v162, v187
	v_add_f32_e32 v68, v100, v101
	v_mov_b32_e32 v65, v70
	s_add_u32 s6, s6, s2
	v_pk_add_f32 v[64:65], v[64:65], v[68:69]
	s_addc_u32 s7, s7, s3
	v_fmac_f32_e32 v65, v64, v66
	v_cvt_pk_bf16_f32 v66, v97, v75
	v_cvt_pk_bf16_f32 v67, v109, v99
	v_cvt_pk_bf16_f32 v68, v103, v77
	v_cvt_pk_bf16_f32 v69, v107, v105
	v_cvt_pk_bf16_f32 v70, v95, v93
	v_cvt_pk_bf16_f32 v71, v91, v89
	v_cvt_pk_bf16_f32 v72, v87, v81
	v_cvt_pk_bf16_f32 v73, v85, v83
	v_cvt_pk_bf16_f32 v74, v96, v74
	v_cvt_pk_bf16_f32 v75, v108, v98
	v_cvt_pk_bf16_f32 v76, v102, v76
	v_cvt_pk_bf16_f32 v77, v106, v104
	v_cvt_pk_bf16_f32 v78, v94, v92
	v_cvt_pk_bf16_f32 v79, v90, v88
	v_cvt_pk_bf16_f32 v80, v86, v80
	v_cvt_pk_bf16_f32 v81, v84, v82
	s_nop 0
	v_permlane32_swap_b32_e32 v66, v68
	v_permlane32_swap_b32_e32 v67, v69
	v_permlane32_swap_b32_e32 v70, v72
	v_permlane32_swap_b32_e32 v71, v73
	v_permlane32_swap_b32_e32 v74, v76
	v_permlane32_swap_b32_e32 v75, v77
	v_permlane32_swap_b32_e32 v78, v80
	v_permlane32_swap_b32_e32 v79, v81
	s_cmp_lg_u32 0, -1
	s_cselect_b32 s2, 0, 0
	s_addk_i32 s2, 0x4000
	v_add_u32_e32 v64, s2, v181
	ds_read_b64_tr_b16 v[82:83], v64 offset:0
	ds_read_b64_tr_b16 v[84:85], v64 offset:0x800
	ds_read_b64_tr_b16 v[86:87], v64 offset:0x1000
	ds_read_b64_tr_b16 v[88:89], v64 offset:0x1800
	ds_read_b64_tr_b16 v[90:91], v64 offset:0x2000
	ds_read_b64_tr_b16 v[92:93], v64 offset:0x2800
	ds_read_b64_tr_b16 v[94:95], v64 offset:0x3000
	ds_read_b64_tr_b16 v[96:97], v64 offset:0x3800
	s_waitcnt lgkmcnt(0)
	s_nop 0
	v_mfma_f32_32x32x16_bf16 v[48:63], v[82:85], v[66:69], v[48:63]
	ds_read_b64_tr_b16 v[82:83], v64 offset:0x200
	ds_read_b64_tr_b16 v[84:85], v64 offset:0xa00
	v_mfma_f32_32x32x16_bf16 v[48:63], v[86:89], v[70:73], v[48:63]
	ds_read_b64_tr_b16 v[86:87], v64 offset:0x1200
	ds_read_b64_tr_b16 v[88:89], v64 offset:0x1a00
	v_mfma_f32_32x32x16_bf16 v[48:63], v[90:93], v[74:77], v[48:63]
	ds_read_b64_tr_b16 v[90:91], v64 offset:0x2200
	ds_read_b64_tr_b16 v[92:93], v64 offset:0x2a00
	v_mfma_f32_32x32x16_bf16 v[48:63], v[94:97], v[78:81], v[48:63]
	ds_read_b64_tr_b16 v[94:95], v64 offset:0x3200
	ds_read_b64_tr_b16 v[96:97], v64 offset:0x3a00
	s_waitcnt lgkmcnt(0)
	v_mfma_f32_32x32x16_bf16 v[32:47], v[82:85], v[66:69], v[32:47]
	ds_read_b64_tr_b16 v[82:83], v64 offset:0x400
	ds_read_b64_tr_b16 v[84:85], v64 offset:0xc00
	v_mfma_f32_32x32x16_bf16 v[32:47], v[86:89], v[70:73], v[32:47]
	ds_read_b64_tr_b16 v[86:87], v64 offset:0x1400
	ds_read_b64_tr_b16 v[88:89], v64 offset:0x1c00
	v_mfma_f32_32x32x16_bf16 v[32:47], v[90:93], v[74:77], v[32:47]
	ds_read_b64_tr_b16 v[90:91], v64 offset:0x2400
	ds_read_b64_tr_b16 v[92:93], v64 offset:0x2c00
	v_mfma_f32_32x32x16_bf16 v[32:47], v[94:97], v[78:81], v[32:47]
	ds_read_b64_tr_b16 v[94:95], v64 offset:0x3400
	ds_read_b64_tr_b16 v[96:97], v64 offset:0x3c00
	s_waitcnt lgkmcnt(0)
	v_mfma_f32_32x32x16_bf16 v[16:31], v[82:85], v[66:69], v[16:31]
	ds_read_b64_tr_b16 v[82:83], v64 offset:0x600
	ds_read_b64_tr_b16 v[84:85], v64 offset:0xe00
	v_mfma_f32_32x32x16_bf16 v[16:31], v[86:89], v[70:73], v[16:31]
	ds_read_b64_tr_b16 v[86:87], v64 offset:0x1600
	ds_read_b64_tr_b16 v[88:89], v64 offset:0x1e00
	v_mfma_f32_32x32x16_bf16 v[16:31], v[90:93], v[74:77], v[16:31]
	ds_read_b64_tr_b16 v[90:91], v64 offset:0x2600
	ds_read_b64_tr_b16 v[92:93], v64 offset:0x2e00
	v_mfma_f32_32x32x16_bf16 v[16:31], v[94:97], v[78:81], v[16:31]
	ds_read_b64_tr_b16 v[94:95], v64 offset:0x3600
	ds_read_b64_tr_b16 v[96:97], v64 offset:0x3e00
	s_waitcnt lgkmcnt(0)
	v_mfma_f32_32x32x16_bf16 v[0:15], v[82:85], v[66:69], v[0:15]
	v_rcp_f32_e32 v67, v65
	v_mbcnt_lo_u32_b32 v66, -1, 0
	v_mbcnt_hi_u32_b32 v66, -1, v66
	s_add_i32 s12, s12, 1
	v_add_u32_e32 v64, s80, v66
	v_ashrrev_i32_e32 v64, 1, v64
	v_mul_f32_e32 v48, v67, v48
	v_mul_f32_e32 v49, v67, v49
	v_bfi_b32 v64, s84, v64, v66
	v_cvt_pk_bf16_f32 v48, v48, v49
	v_mul_f32_e32 v49, v67, v50
	v_mul_f32_e32 v50, v67, v51
	v_ashrrev_i32_e32 v65, 31, v64
	v_cvt_pk_bf16_f32 v49, v49, v50
	v_mul_f32_e32 v50, v67, v52
	v_mul_f32_e32 v51, v67, v53
	v_lshlrev_b64 v[64:65], 12, v[64:65]
	v_lshrrev_b32_e32 v66, 1, v66
	v_cvt_pk_bf16_f32 v50, v50, v51
	v_mul_f32_e32 v51, v67, v54
	v_lshl_add_u64 v[64:65], s[6:7], 0, v[64:65]
	v_and_b32_e32 v128, 16, v66
	v_mul_f32_e32 v52, v67, v55
	v_cvt_pk_bf16_f32 v51, v51, v52
	v_lshl_add_u64 v[64:65], v[64:65], 0, v[128:129]
	v_permlane32_swap_b32_e32 v48, v50
	v_permlane32_swap_b32_e32 v49, v51
	global_store_dwordx4 v[64:65], v[48:51], off sc1
	v_mfma_f32_32x32x16_bf16 v[0:15], v[86:89], v[70:73], v[0:15]
	v_mul_f32_e32 v52, v67, v63
	v_mul_f32_e32 v48, v67, v56
	v_mul_f32_e32 v49, v67, v57
	v_cvt_pk_bf16_f32 v48, v48, v49
	v_mul_f32_e32 v49, v67, v58
	v_mul_f32_e32 v50, v67, v59
	v_cvt_pk_bf16_f32 v49, v49, v50
	v_mul_f32_e32 v50, v67, v60
	v_mul_f32_e32 v51, v67, v61
	v_cvt_pk_bf16_f32 v50, v50, v51
	v_mul_f32_e32 v51, v67, v62
	v_cvt_pk_bf16_f32 v51, v51, v52
	v_permlane32_swap_b32_e32 v48, v50
	s_nop 0
	v_permlane32_swap_b32_e32 v49, v51
	v_mul_f32_e32 v32, v67, v32
	v_mul_f32_e32 v33, v67, v33
	global_store_dwordx4 v[64:65], v[48:51], off offset:32 sc1
	v_cvt_pk_bf16_f32 v32, v32, v33
	v_mul_f32_e32 v33, v67, v34
	v_mul_f32_e32 v34, v67, v35
	v_cvt_pk_bf16_f32 v33, v33, v34
	v_mul_f32_e32 v34, v67, v36
	v_mul_f32_e32 v35, v67, v37
	v_cvt_pk_bf16_f32 v34, v34, v35
	v_mul_f32_e32 v35, v67, v38
	v_mul_f32_e32 v36, v67, v39
	v_cvt_pk_bf16_f32 v35, v35, v36
	v_permlane32_swap_b32_e32 v32, v34
	v_permlane32_swap_b32_e32 v33, v35
	v_mfma_f32_32x32x16_bf16 v[0:15], v[90:93], v[74:77], v[0:15]
	global_store_dwordx4 v[64:65], v[32:35], off offset:64 sc1
	v_mul_f32_e32 v36, v67, v47
	v_mul_f32_e32 v16, v67, v16
	v_mul_f32_e32 v32, v67, v40
	v_mul_f32_e32 v33, v67, v41
	v_cvt_pk_bf16_f32 v32, v32, v33
	v_mul_f32_e32 v33, v67, v42
	v_mul_f32_e32 v34, v67, v43
	v_cvt_pk_bf16_f32 v33, v33, v34
	v_mul_f32_e32 v34, v67, v44
	v_mul_f32_e32 v35, v67, v45
	v_cvt_pk_bf16_f32 v34, v34, v35
	v_mul_f32_e32 v35, v67, v46
	v_cvt_pk_bf16_f32 v35, v35, v36
	v_permlane32_swap_b32_e32 v32, v34
	s_nop 0
	v_permlane32_swap_b32_e32 v33, v35
	v_mul_f32_e32 v17, v67, v17
	global_store_dwordx4 v[64:65], v[32:35], off offset:96 sc1
	v_cvt_pk_bf16_f32 v16, v16, v17
	v_mul_f32_e32 v17, v67, v18
	v_mul_f32_e32 v18, v67, v19
	v_cvt_pk_bf16_f32 v17, v17, v18
	v_mul_f32_e32 v18, v67, v20
	v_mul_f32_e32 v19, v67, v21
	v_mfma_f32_32x32x16_bf16 v[0:15], v[94:97], v[78:81], v[0:15]
	v_cvt_pk_bf16_f32 v18, v18, v19
	v_mul_f32_e32 v19, v67, v22
	v_mul_f32_e32 v20, v67, v23
	v_cvt_pk_bf16_f32 v19, v19, v20
	v_permlane32_swap_b32_e32 v16, v18
	v_permlane32_swap_b32_e32 v17, v19
	global_store_dwordx4 v[64:65], v[16:19], off offset:128 sc1
	v_mul_f32_e32 v20, v67, v31
	s_nop 5
	v_mul_f32_e32 v0, v67, v0
	v_mul_f32_e32 v16, v67, v24
	v_mul_f32_e32 v17, v67, v25
	v_cvt_pk_bf16_f32 v16, v16, v17
	v_mul_f32_e32 v17, v67, v26
	v_mul_f32_e32 v18, v67, v27
	v_cvt_pk_bf16_f32 v17, v17, v18
	v_mul_f32_e32 v18, v67, v28
	v_mul_f32_e32 v19, v67, v29
	v_cvt_pk_bf16_f32 v18, v18, v19
	v_mul_f32_e32 v19, v67, v30
	v_cvt_pk_bf16_f32 v19, v19, v20
	v_permlane32_swap_b32_e32 v16, v18
	s_nop 0
	v_permlane32_swap_b32_e32 v17, v19
	v_mul_f32_e32 v1, v67, v1
	global_store_dwordx4 v[64:65], v[16:19], off offset:160 sc1
	v_cvt_pk_bf16_f32 v0, v0, v1
	v_mul_f32_e32 v1, v67, v2
	v_mul_f32_e32 v2, v67, v3
	v_cvt_pk_bf16_f32 v1, v1, v2
	v_mul_f32_e32 v2, v67, v4
	v_mul_f32_e32 v3, v67, v5
	v_cvt_pk_bf16_f32 v2, v2, v3
	v_mul_f32_e32 v3, v67, v6
	v_mul_f32_e32 v4, v67, v7
	v_cvt_pk_bf16_f32 v3, v3, v4
	v_permlane32_swap_b32_e32 v0, v2
	v_permlane32_swap_b32_e32 v1, v3
	global_store_dwordx4 v[64:65], v[0:3], off offset:192 sc1
	v_mul_f32_e32 v4, v67, v15
	s_mov_b64 s[6:7], 0
	v_mul_f32_e32 v0, v67, v8
	v_mul_f32_e32 v1, v67, v9
	v_cvt_pk_bf16_f32 v0, v0, v1
	v_mul_f32_e32 v1, v67, v10
	v_mul_f32_e32 v2, v67, v11
	v_cvt_pk_bf16_f32 v1, v1, v2
	v_mul_f32_e32 v2, v67, v12
	v_mul_f32_e32 v3, v67, v13
	v_cvt_pk_bf16_f32 v2, v2, v3
	v_mul_f32_e32 v3, v67, v14
	v_cvt_pk_bf16_f32 v3, v3, v4
	v_permlane32_swap_b32_e32 v0, v2
	s_nop 0
	v_permlane32_swap_b32_e32 v1, v3
	global_store_dwordx4 v[64:65], v[0:3], off offset:224 sc1

.LBB0_851:
	v_exp_f32_e32 v101, v80
	v_exp_f32_e32 v103, v81
	v_exp_f32_e32 v111, v88
	v_exp_f32_e32 v89, v89
	v_exp_f32_e32 v105, v82
	v_exp_f32_e32 v113, v90
	v_exp_f32_e32 v83, v83
	v_exp_f32_e32 v91, v91
	v_exp_f32_e32 v107, v84
	v_exp_f32_e32 v115, v92
	v_mov_b32_e32 v100, v64
	v_mov_b32_e32 v102, v65
	v_mov_b32_e32 v110, v72
	v_mov_b32_e32 v88, v73
	v_exp_f32_e32 v85, v85
	v_exp_f32_e32 v93, v93
	v_pk_add_f32 v[80:81], v[100:101], v[102:103]
	v_pk_add_f32 v[118:119], v[110:111], v[88:89]
	v_mov_b32_e32 v104, v66
	v_mov_b32_e32 v112, v74
	v_exp_f32_e32 v109, v86
	v_exp_f32_e32 v117, v94
	v_pk_add_f32 v[80:81], v[104:105], v[80:81]
	v_pk_add_f32 v[118:119], v[112:113], v[118:119]
	v_mov_b32_e32 v82, v67
	v_mov_b32_e32 v90, v75
	v_exp_f32_e32 v87, v87
	v_exp_f32_e32 v95, v95
	v_pk_add_f32 v[80:81], v[82:83], v[80:81]
	v_pk_add_f32 v[118:119], v[90:91], v[118:119]
	v_mov_b32_e32 v106, v68
	v_mov_b32_e32 v114, v76
	v_pk_add_f32 v[80:81], v[106:107], v[80:81]
	v_pk_add_f32 v[118:119], v[114:115], v[118:119]
	v_mov_b32_e32 v84, v69
	v_mov_b32_e32 v92, v77
	v_pk_add_f32 v[80:81], v[84:85], v[80:81]
	v_pk_add_f32 v[118:119], v[92:93], v[118:119]
	v_mov_b32_e32 v108, v70
	v_mov_b32_e32 v116, v78
	v_pk_add_f32 v[80:81], v[108:109], v[80:81]
	v_pk_add_f32 v[118:119], v[116:117], v[118:119]
	v_mov_b32_e32 v86, v71
	v_mov_b32_e32 v94, v79
	v_pk_add_f32 v[80:81], v[86:87], v[80:81]
	v_pk_add_f32 v[118:119], v[94:95], v[118:119]
	s_lshl_b32 s2, s63, 12
	v_pk_add_f32 v[80:81], v[118:119], v[80:81]
	s_add_u32 s16, s35, s2
	v_pk_add_f32 v[80:81], v[80:81], v[80:81] op_sel:[0,1] op_sel_hi:[1,0]
	s_addc_u32 s17, s36, 0
	s_lshl_b32 s2, s33, 7
	v_mov_b32_e32 v99, v80
	s_ashr_i32 s3, s2, 31
	s_nop 0
	v_permlane32_swap_b32_e32 v80, v99
	s_lshl_b64 s[2:3], s[2:3], 1
	v_mul_f32_e32 v96, v210, v200
	v_add_f32_e32 v98, v142, v143
	v_mov_b32_e32 v97, v80
	s_add_u32 s16, s16, s2
	v_pk_add_f32 v[80:81], v[96:97], v[98:99]
	v_cvt_pk_bf16_f32 v64, v64, v65
	v_cvt_pk_bf16_f32 v65, v66, v67
	v_cvt_pk_bf16_f32 v66, v68, v69
	v_cvt_pk_bf16_f32 v67, v70, v71
	v_cvt_pk_bf16_f32 v68, v72, v73
	v_cvt_pk_bf16_f32 v69, v74, v75
	v_cvt_pk_bf16_f32 v70, v76, v77
	v_cvt_pk_bf16_f32 v71, v78, v79
	v_cvt_pk_bf16_f32 v72, v101, v103
	v_cvt_pk_bf16_f32 v73, v105, v83
	v_cvt_pk_bf16_f32 v74, v107, v85
	v_cvt_pk_bf16_f32 v75, v109, v87
	v_cvt_pk_bf16_f32 v76, v111, v89
	v_cvt_pk_bf16_f32 v77, v113, v91
	v_cvt_pk_bf16_f32 v78, v115, v93
	v_cvt_pk_bf16_f32 v79, v117, v95
	s_addc_u32 s17, s17, s3
	v_fmac_f32_e32 v81, v80, v128
	v_permlane32_swap_b32_e32 v64, v66
	v_permlane32_swap_b32_e32 v65, v67
	v_permlane32_swap_b32_e32 v68, v70
	v_permlane32_swap_b32_e32 v69, v71
	v_permlane32_swap_b32_e32 v72, v74
	v_permlane32_swap_b32_e32 v73, v75
	v_permlane32_swap_b32_e32 v76, v78
	v_permlane32_swap_b32_e32 v77, v79
	ds_read_b64_tr_b16 v[82:83], v203 offset:0
	ds_read_b64_tr_b16 v[84:85], v203 offset:0x800
	ds_read_b64_tr_b16 v[86:87], v203 offset:0x1000
	ds_read_b64_tr_b16 v[88:89], v203 offset:0x1800
	ds_read_b64_tr_b16 v[90:91], v203 offset:0x2000
	ds_read_b64_tr_b16 v[92:93], v203 offset:0x2800
	ds_read_b64_tr_b16 v[94:95], v203 offset:0x3000
	ds_read_b64_tr_b16 v[96:97], v203 offset:0x3800
	s_waitcnt lgkmcnt(0)
	s_nop 0
	v_mfma_f32_32x32x16_bf16 v[0:15], v[82:85], v[64:67], v[0:15]
	ds_read_b64_tr_b16 v[82:83], v203 offset:0x200
	ds_read_b64_tr_b16 v[84:85], v203 offset:0xa00
	v_mfma_f32_32x32x16_bf16 v[0:15], v[86:89], v[68:71], v[0:15]
	ds_read_b64_tr_b16 v[86:87], v203 offset:0x1200
	ds_read_b64_tr_b16 v[88:89], v203 offset:0x1a00
	v_mfma_f32_32x32x16_bf16 v[0:15], v[90:93], v[72:75], v[0:15]
	ds_read_b64_tr_b16 v[90:91], v203 offset:0x2200
	ds_read_b64_tr_b16 v[92:93], v203 offset:0x2a00
	v_mfma_f32_32x32x16_bf16 v[0:15], v[94:97], v[76:79], v[0:15]
	ds_read_b64_tr_b16 v[94:95], v203 offset:0x3200
	ds_read_b64_tr_b16 v[96:97], v203 offset:0x3a00
	s_waitcnt lgkmcnt(0)
	v_mfma_f32_32x32x16_bf16 v[48:63], v[82:85], v[64:67], v[48:63]
	ds_read_b64_tr_b16 v[82:83], v203 offset:0x400
	ds_read_b64_tr_b16 v[84:85], v203 offset:0xc00
	v_mfma_f32_32x32x16_bf16 v[48:63], v[86:89], v[68:71], v[48:63]
	ds_read_b64_tr_b16 v[86:87], v203 offset:0x1400
	ds_read_b64_tr_b16 v[88:89], v203 offset:0x1c00
	v_mfma_f32_32x32x16_bf16 v[48:63], v[90:93], v[72:75], v[48:63]
	ds_read_b64_tr_b16 v[90:91], v203 offset:0x2400
	ds_read_b64_tr_b16 v[92:93], v203 offset:0x2c00
	v_mfma_f32_32x32x16_bf16 v[48:63], v[94:97], v[76:79], v[48:63]
	ds_read_b64_tr_b16 v[94:95], v203 offset:0x3400
	ds_read_b64_tr_b16 v[96:97], v203 offset:0x3c00
	s_waitcnt lgkmcnt(0)
	v_mfma_f32_32x32x16_bf16 v[32:47], v[82:85], v[64:67], v[32:47]
	ds_read_b64_tr_b16 v[82:83], v203 offset:0x600
	ds_read_b64_tr_b16 v[84:85], v203 offset:0xe00
	v_mfma_f32_32x32x16_bf16 v[32:47], v[86:89], v[68:71], v[32:47]
	ds_read_b64_tr_b16 v[86:87], v203 offset:0x1600
	ds_read_b64_tr_b16 v[88:89], v203 offset:0x1e00
	v_mfma_f32_32x32x16_bf16 v[32:47], v[90:93], v[72:75], v[32:47]
	ds_read_b64_tr_b16 v[90:91], v203 offset:0x2600
	ds_read_b64_tr_b16 v[92:93], v203 offset:0x2e00
	v_mfma_f32_32x32x16_bf16 v[32:47], v[94:97], v[76:79], v[32:47]
	ds_read_b64_tr_b16 v[94:95], v203 offset:0x3600
	ds_read_b64_tr_b16 v[96:97], v203 offset:0x3e00
	s_waitcnt lgkmcnt(0)
	v_mfma_f32_32x32x16_bf16 v[16:31], v[82:85], v[64:67], v[16:31]
	v_rcp_f32_e32 v67, v81
	v_mbcnt_lo_u32_b32 v66, -1, 0
	v_mbcnt_hi_u32_b32 v66, -1, v66
	s_add_i32 s91, s91, 1
	v_add_u32_e32 v64, s80, v66
	v_ashrrev_i32_e32 v64, 1, v64
	v_mul_f32_e32 v0, v67, v0
	v_mul_f32_e32 v1, v67, v1
	v_bfi_b32 v64, s84, v64, v66
	v_cvt_pk_bf16_f32 v0, v0, v1
	v_mul_f32_e32 v1, v67, v2
	v_mul_f32_e32 v2, v67, v3
	v_ashrrev_i32_e32 v65, 31, v64
	v_cvt_pk_bf16_f32 v1, v1, v2
	v_mul_f32_e32 v2, v67, v4
	v_mul_f32_e32 v3, v67, v5
	v_lshlrev_b64 v[64:65], 12, v[64:65]
	v_lshrrev_b32_e32 v66, 1, v66
	v_cvt_pk_bf16_f32 v2, v2, v3
	v_mul_f32_e32 v3, v67, v6
	v_lshl_add_u64 v[64:65], s[16:17], 0, v[64:65]
	v_and_b32_e32 v128, 16, v66
	v_mul_f32_e32 v4, v67, v7
	v_cvt_pk_bf16_f32 v3, v3, v4
	v_lshl_add_u64 v[64:65], v[64:65], 0, v[128:129]
	v_permlane32_swap_b32_e32 v0, v2
	v_permlane32_swap_b32_e32 v1, v3
	global_store_dwordx4 v[64:65], v[0:3], off sc1
	v_mul_f32_e32 v4, v67, v15
	v_mfma_f32_32x32x16_bf16 v[16:31], v[86:89], v[68:71], v[16:31]
	v_mul_f32_e32 v0, v67, v8
	v_mul_f32_e32 v1, v67, v9
	v_cvt_pk_bf16_f32 v0, v0, v1
	v_mul_f32_e32 v1, v67, v10
	v_mul_f32_e32 v2, v67, v11
	v_cvt_pk_bf16_f32 v1, v1, v2
	v_mul_f32_e32 v2, v67, v12
	v_mul_f32_e32 v3, v67, v13
	v_cvt_pk_bf16_f32 v2, v2, v3
	v_mul_f32_e32 v3, v67, v14
	v_cvt_pk_bf16_f32 v3, v3, v4
	v_permlane32_swap_b32_e32 v0, v2
	s_nop 0
	v_permlane32_swap_b32_e32 v1, v3
	global_store_dwordx4 v[64:65], v[0:3], off offset:32 sc1
	v_mul_f32_e32 v4, v67, v55
	v_mfma_f32_32x32x16_bf16 v[16:31], v[90:93], v[72:75], v[16:31]
	v_mul_f32_e32 v0, v67, v48
	v_mul_f32_e32 v1, v67, v49
	v_cvt_pk_bf16_f32 v0, v0, v1
	v_mul_f32_e32 v1, v67, v50
	v_mul_f32_e32 v2, v67, v51
	v_cvt_pk_bf16_f32 v1, v1, v2
	v_mul_f32_e32 v2, v67, v52
	v_mul_f32_e32 v3, v67, v53
	v_cvt_pk_bf16_f32 v2, v2, v3
	v_mul_f32_e32 v3, v67, v54
	v_cvt_pk_bf16_f32 v3, v3, v4
	v_permlane32_swap_b32_e32 v0, v2
	s_nop 0
	v_permlane32_swap_b32_e32 v1, v3
	global_store_dwordx4 v[64:65], v[0:3], off offset:64 sc1
	v_mul_f32_e32 v4, v67, v63
	v_mfma_f32_32x32x16_bf16 v[16:31], v[94:97], v[76:79], v[16:31]
	v_mul_f32_e32 v0, v67, v56
	v_mul_f32_e32 v1, v67, v57
	v_cvt_pk_bf16_f32 v0, v0, v1
	v_mul_f32_e32 v1, v67, v58
	v_mul_f32_e32 v2, v67, v59
	v_cvt_pk_bf16_f32 v1, v1, v2
	v_mul_f32_e32 v2, v67, v60
	v_mul_f32_e32 v3, v67, v61
	v_cvt_pk_bf16_f32 v2, v2, v3
	v_mul_f32_e32 v3, v67, v62
	v_cvt_pk_bf16_f32 v3, v3, v4
	v_permlane32_swap_b32_e32 v0, v2
	s_nop 0
	v_permlane32_swap_b32_e32 v1, v3
	global_store_dwordx4 v[64:65], v[0:3], off offset:96 sc1
	v_mul_f32_e32 v4, v67, v39
	s_lshl_b32 s2, s91, 8
	v_mul_f32_e32 v0, v67, v32
	v_mul_f32_e32 v1, v67, v33
	v_cvt_pk_bf16_f32 v0, v0, v1
	v_mul_f32_e32 v1, v67, v34
	v_mul_f32_e32 v2, v67, v35
	v_cvt_pk_bf16_f32 v1, v1, v2
	v_mul_f32_e32 v2, v67, v36
	v_mul_f32_e32 v3, v67, v37
	v_cvt_pk_bf16_f32 v2, v2, v3
	v_mul_f32_e32 v3, v67, v38
	v_cvt_pk_bf16_f32 v3, v3, v4
	v_permlane32_swap_b32_e32 v0, v2
	s_nop 0
	v_permlane32_swap_b32_e32 v1, v3
	global_store_dwordx4 v[64:65], v[0:3], off offset:128 sc1
	v_mul_f32_e32 v4, v67, v47
	s_add_i32 s3, s2, s94
	v_mul_f32_e32 v0, v67, v40
	v_mul_f32_e32 v1, v67, v41
	v_cvt_pk_bf16_f32 v0, v0, v1
	v_mul_f32_e32 v1, v67, v42
	v_mul_f32_e32 v2, v67, v43
	v_cvt_pk_bf16_f32 v1, v1, v2
	v_mul_f32_e32 v2, v67, v44
	v_mul_f32_e32 v3, v67, v45
	v_cvt_pk_bf16_f32 v2, v2, v3
	v_mul_f32_e32 v3, v67, v46
	v_cvt_pk_bf16_f32 v3, v3, v4
	v_permlane32_swap_b32_e32 v0, v2
	s_nop 0
	v_permlane32_swap_b32_e32 v1, v3
	global_store_dwordx4 v[64:65], v[0:3], off offset:160 sc1
	v_mul_f32_e32 v4, v67, v23
	s_cmp_lt_i32 s3, s37
	v_mul_f32_e32 v0, v67, v16
	v_mul_f32_e32 v1, v67, v17
	v_cvt_pk_bf16_f32 v0, v0, v1
	v_mul_f32_e32 v1, v67, v18
	v_mul_f32_e32 v2, v67, v19
	v_cvt_pk_bf16_f32 v1, v1, v2
	v_mul_f32_e32 v2, v67, v20
	v_mul_f32_e32 v3, v67, v21
	v_cvt_pk_bf16_f32 v2, v2, v3
	v_mul_f32_e32 v3, v67, v22
	v_cvt_pk_bf16_f32 v3, v3, v4
	v_permlane32_swap_b32_e32 v0, v2
	s_nop 0
	v_permlane32_swap_b32_e32 v1, v3
	global_store_dwordx4 v[64:65], v[0:3], off offset:192 sc1
	v_mul_f32_e32 v4, v67, v31
	s_nop 0
	v_mul_f32_e32 v0, v67, v24
	v_mul_f32_e32 v1, v67, v25
	v_cvt_pk_bf16_f32 v0, v0, v1
	v_mul_f32_e32 v1, v67, v26
	v_mul_f32_e32 v2, v67, v27
	v_cvt_pk_bf16_f32 v1, v1, v2
	v_mul_f32_e32 v2, v67, v28
	v_mul_f32_e32 v3, v67, v29
	v_cvt_pk_bf16_f32 v2, v2, v3
	v_mul_f32_e32 v3, v67, v30
	v_cvt_pk_bf16_f32 v3, v3, v4
	v_permlane32_swap_b32_e32 v0, v2
	s_nop 0
	v_permlane32_swap_b32_e32 v1, v3
	global_store_dwordx4 v[64:65], v[0:3], off offset:224 sc1
	s_cbranch_scc0 .LBB0_904

.LBB0_873:
	v_exp_f32_e32 v101, v80
	v_exp_f32_e32 v103, v81
	v_exp_f32_e32 v111, v88
	v_exp_f32_e32 v89, v89
	v_exp_f32_e32 v105, v82
	v_exp_f32_e32 v113, v90
	v_exp_f32_e32 v83, v83
	v_exp_f32_e32 v91, v91
	v_exp_f32_e32 v107, v84
	v_exp_f32_e32 v115, v92
	v_mov_b32_e32 v100, v64
	v_mov_b32_e32 v102, v65
	v_mov_b32_e32 v110, v72
	v_mov_b32_e32 v88, v73
	v_exp_f32_e32 v85, v85
	v_exp_f32_e32 v93, v93
	v_pk_add_f32 v[80:81], v[100:101], v[102:103]
	v_pk_add_f32 v[118:119], v[110:111], v[88:89]
	v_mov_b32_e32 v104, v66
	v_mov_b32_e32 v112, v74
	v_exp_f32_e32 v109, v86
	v_exp_f32_e32 v117, v94
	v_pk_add_f32 v[80:81], v[104:105], v[80:81]
	v_pk_add_f32 v[118:119], v[112:113], v[118:119]
	v_mov_b32_e32 v82, v67
	v_mov_b32_e32 v90, v75
	v_exp_f32_e32 v87, v87
	v_exp_f32_e32 v95, v95
	v_pk_add_f32 v[80:81], v[82:83], v[80:81]
	v_pk_add_f32 v[118:119], v[90:91], v[118:119]
	v_mov_b32_e32 v106, v68
	v_mov_b32_e32 v114, v76
	v_pk_add_f32 v[80:81], v[106:107], v[80:81]
	v_pk_add_f32 v[118:119], v[114:115], v[118:119]
	v_mov_b32_e32 v84, v69
	v_mov_b32_e32 v92, v77
	v_pk_add_f32 v[80:81], v[84:85], v[80:81]
	v_pk_add_f32 v[118:119], v[92:93], v[118:119]
	v_mov_b32_e32 v108, v70
	v_mov_b32_e32 v116, v78
	v_pk_add_f32 v[80:81], v[108:109], v[80:81]
	v_pk_add_f32 v[118:119], v[116:117], v[118:119]
	v_mov_b32_e32 v86, v71
	v_mov_b32_e32 v94, v79
	v_pk_add_f32 v[80:81], v[86:87], v[80:81]
	v_pk_add_f32 v[118:119], v[94:95], v[118:119]
	s_lshl_b32 s2, s33, 12
	v_pk_add_f32 v[80:81], v[118:119], v[80:81]
	s_add_u32 s8, s35, s2
	v_pk_add_f32 v[80:81], v[80:81], v[80:81] op_sel:[0,1] op_sel_hi:[1,0]
	s_addc_u32 s9, s36, 0
	s_lshl_b32 s2, s28, 7
	v_mov_b32_e32 v99, v80
	s_ashr_i32 s3, s2, 31
	s_nop 0
	v_permlane32_swap_b32_e32 v80, v99
	s_lshl_b64 s[2:3], s[2:3], 1
	v_mul_f32_e32 v96, v217, v208
	v_add_f32_e32 v98, v142, v143
	v_mov_b32_e32 v97, v80
	s_add_u32 s8, s8, s2
	v_pk_add_f32 v[80:81], v[96:97], v[98:99]
	v_cvt_pk_bf16_f32 v64, v64, v65
	v_cvt_pk_bf16_f32 v65, v66, v67
	v_cvt_pk_bf16_f32 v66, v68, v69
	v_cvt_pk_bf16_f32 v67, v70, v71
	v_cvt_pk_bf16_f32 v68, v72, v73
	v_cvt_pk_bf16_f32 v69, v74, v75
	v_cvt_pk_bf16_f32 v70, v76, v77
	v_cvt_pk_bf16_f32 v71, v78, v79
	v_cvt_pk_bf16_f32 v72, v101, v103
	v_cvt_pk_bf16_f32 v73, v105, v83
	v_cvt_pk_bf16_f32 v74, v107, v85
	v_cvt_pk_bf16_f32 v75, v109, v87
	v_cvt_pk_bf16_f32 v76, v111, v89
	v_cvt_pk_bf16_f32 v77, v113, v91
	v_cvt_pk_bf16_f32 v78, v115, v93
	v_cvt_pk_bf16_f32 v79, v117, v95
	s_addc_u32 s9, s9, s3
	v_fmac_f32_e32 v81, v80, v128
	v_permlane32_swap_b32_e32 v64, v66
	v_permlane32_swap_b32_e32 v65, v67
	v_permlane32_swap_b32_e32 v68, v70
	v_permlane32_swap_b32_e32 v69, v71
	v_permlane32_swap_b32_e32 v72, v74
	v_permlane32_swap_b32_e32 v73, v75
	v_permlane32_swap_b32_e32 v76, v78
	v_permlane32_swap_b32_e32 v77, v79
	ds_read_b64_tr_b16 v[82:83], v211 offset:0
	ds_read_b64_tr_b16 v[84:85], v211 offset:0x800
	ds_read_b64_tr_b16 v[86:87], v211 offset:0x1000
	ds_read_b64_tr_b16 v[88:89], v211 offset:0x1800
	ds_read_b64_tr_b16 v[90:91], v211 offset:0x2000
	ds_read_b64_tr_b16 v[92:93], v211 offset:0x2800
	ds_read_b64_tr_b16 v[94:95], v211 offset:0x3000
	ds_read_b64_tr_b16 v[96:97], v211 offset:0x3800
	s_waitcnt lgkmcnt(0)
	s_nop 0
	v_mfma_f32_32x32x16_bf16 v[0:15], v[82:85], v[64:67], v[0:15]
	ds_read_b64_tr_b16 v[82:83], v211 offset:0x200
	ds_read_b64_tr_b16 v[84:85], v211 offset:0xa00
	v_mfma_f32_32x32x16_bf16 v[0:15], v[86:89], v[68:71], v[0:15]
	ds_read_b64_tr_b16 v[86:87], v211 offset:0x1200
	ds_read_b64_tr_b16 v[88:89], v211 offset:0x1a00
	v_mfma_f32_32x32x16_bf16 v[0:15], v[90:93], v[72:75], v[0:15]
	ds_read_b64_tr_b16 v[90:91], v211 offset:0x2200
	ds_read_b64_tr_b16 v[92:93], v211 offset:0x2a00
	v_mfma_f32_32x32x16_bf16 v[0:15], v[94:97], v[76:79], v[0:15]
	ds_read_b64_tr_b16 v[94:95], v211 offset:0x3200
	ds_read_b64_tr_b16 v[96:97], v211 offset:0x3a00
	s_waitcnt lgkmcnt(0)
	v_mfma_f32_32x32x16_bf16 v[48:63], v[82:85], v[64:67], v[48:63]
	ds_read_b64_tr_b16 v[82:83], v211 offset:0x400
	ds_read_b64_tr_b16 v[84:85], v211 offset:0xc00
	v_mfma_f32_32x32x16_bf16 v[48:63], v[86:89], v[68:71], v[48:63]
	ds_read_b64_tr_b16 v[86:87], v211 offset:0x1400
	ds_read_b64_tr_b16 v[88:89], v211 offset:0x1c00
	v_mfma_f32_32x32x16_bf16 v[48:63], v[90:93], v[72:75], v[48:63]
	ds_read_b64_tr_b16 v[90:91], v211 offset:0x2400
	ds_read_b64_tr_b16 v[92:93], v211 offset:0x2c00
	v_mfma_f32_32x32x16_bf16 v[48:63], v[94:97], v[76:79], v[48:63]
	ds_read_b64_tr_b16 v[94:95], v211 offset:0x3400
	ds_read_b64_tr_b16 v[96:97], v211 offset:0x3c00
	s_waitcnt lgkmcnt(0)
	v_mfma_f32_32x32x16_bf16 v[32:47], v[82:85], v[64:67], v[32:47]
	ds_read_b64_tr_b16 v[82:83], v211 offset:0x600
	ds_read_b64_tr_b16 v[84:85], v211 offset:0xe00
	v_mfma_f32_32x32x16_bf16 v[32:47], v[86:89], v[68:71], v[32:47]
	ds_read_b64_tr_b16 v[86:87], v211 offset:0x1600
	ds_read_b64_tr_b16 v[88:89], v211 offset:0x1e00
	v_mfma_f32_32x32x16_bf16 v[32:47], v[90:93], v[72:75], v[32:47]
	ds_read_b64_tr_b16 v[90:91], v211 offset:0x2600
	ds_read_b64_tr_b16 v[92:93], v211 offset:0x2e00
	v_mfma_f32_32x32x16_bf16 v[32:47], v[94:97], v[76:79], v[32:47]
	ds_read_b64_tr_b16 v[94:95], v211 offset:0x3600
	ds_read_b64_tr_b16 v[96:97], v211 offset:0x3e00
	s_waitcnt lgkmcnt(0)
	v_mfma_f32_32x32x16_bf16 v[16:31], v[82:85], v[64:67], v[16:31]
	v_rcp_f32_e32 v67, v81
	v_mbcnt_lo_u32_b32 v66, -1, 0
	v_mbcnt_hi_u32_b32 v66, -1, v66
	s_add_i32 s20, s20, 1
	v_add_u32_e32 v64, s80, v66
	v_ashrrev_i32_e32 v64, 1, v64
	v_mul_f32_e32 v0, v67, v0
	v_mul_f32_e32 v1, v67, v1
	v_bfi_b32 v64, s84, v64, v66
	v_cvt_pk_bf16_f32 v0, v0, v1
	v_mul_f32_e32 v1, v67, v2
	v_mul_f32_e32 v2, v67, v3
	v_ashrrev_i32_e32 v65, 31, v64
	v_cvt_pk_bf16_f32 v1, v1, v2
	v_mul_f32_e32 v2, v67, v4
	v_mul_f32_e32 v3, v67, v5
	v_lshlrev_b64 v[64:65], 12, v[64:65]
	v_lshrrev_b32_e32 v66, 1, v66
	v_cvt_pk_bf16_f32 v2, v2, v3
	v_mul_f32_e32 v3, v67, v6
	v_lshl_add_u64 v[64:65], s[8:9], 0, v[64:65]
	v_and_b32_e32 v128, 16, v66
	v_mul_f32_e32 v4, v67, v7
	v_cvt_pk_bf16_f32 v3, v3, v4
	v_lshl_add_u64 v[64:65], v[64:65], 0, v[128:129]
	v_permlane32_swap_b32_e32 v0, v2
	v_permlane32_swap_b32_e32 v1, v3
	global_store_dwordx4 v[64:65], v[0:3], off sc1
	v_mul_f32_e32 v4, v67, v15
	v_mfma_f32_32x32x16_bf16 v[16:31], v[86:89], v[68:71], v[16:31]
	v_mul_f32_e32 v0, v67, v8
	v_mul_f32_e32 v1, v67, v9
	v_cvt_pk_bf16_f32 v0, v0, v1
	v_mul_f32_e32 v1, v67, v10
	v_mul_f32_e32 v2, v67, v11
	v_cvt_pk_bf16_f32 v1, v1, v2
	v_mul_f32_e32 v2, v67, v12
	v_mul_f32_e32 v3, v67, v13
	v_cvt_pk_bf16_f32 v2, v2, v3
	v_mul_f32_e32 v3, v67, v14
	v_cvt_pk_bf16_f32 v3, v3, v4
	v_permlane32_swap_b32_e32 v0, v2
	s_nop 0
	v_permlane32_swap_b32_e32 v1, v3
	global_store_dwordx4 v[64:65], v[0:3], off offset:32 sc1
	v_mul_f32_e32 v4, v67, v55
	v_mfma_f32_32x32x16_bf16 v[16:31], v[90:93], v[72:75], v[16:31]
	v_mul_f32_e32 v0, v67, v48
	v_mul_f32_e32 v1, v67, v49
	v_cvt_pk_bf16_f32 v0, v0, v1
	v_mul_f32_e32 v1, v67, v50
	v_mul_f32_e32 v2, v67, v51
	v_cvt_pk_bf16_f32 v1, v1, v2
	v_mul_f32_e32 v2, v67, v52
	v_mul_f32_e32 v3, v67, v53
	v_cvt_pk_bf16_f32 v2, v2, v3
	v_mul_f32_e32 v3, v67, v54
	v_cvt_pk_bf16_f32 v3, v3, v4
	v_permlane32_swap_b32_e32 v0, v2
	s_nop 0
	v_permlane32_swap_b32_e32 v1, v3
	global_store_dwordx4 v[64:65], v[0:3], off offset:64 sc1
	v_mul_f32_e32 v4, v67, v63
	v_mfma_f32_32x32x16_bf16 v[16:31], v[94:97], v[76:79], v[16:31]
	v_mul_f32_e32 v0, v67, v56
	v_mul_f32_e32 v1, v67, v57
	v_cvt_pk_bf16_f32 v0, v0, v1
	v_mul_f32_e32 v1, v67, v58
	v_mul_f32_e32 v2, v67, v59
	v_cvt_pk_bf16_f32 v1, v1, v2
	v_mul_f32_e32 v2, v67, v60
	v_mul_f32_e32 v3, v67, v61
	v_cvt_pk_bf16_f32 v2, v2, v3
	v_mul_f32_e32 v3, v67, v62
	v_cvt_pk_bf16_f32 v3, v3, v4
	v_permlane32_swap_b32_e32 v0, v2
	s_nop 0
	v_permlane32_swap_b32_e32 v1, v3
	global_store_dwordx4 v[64:65], v[0:3], off offset:96 sc1
	v_mul_f32_e32 v4, v67, v39
	s_lshl_b32 s2, s20, 8
	v_mul_f32_e32 v0, v67, v32
	v_mul_f32_e32 v1, v67, v33
	v_cvt_pk_bf16_f32 v0, v0, v1
	v_mul_f32_e32 v1, v67, v34
	v_mul_f32_e32 v2, v67, v35
	v_cvt_pk_bf16_f32 v1, v1, v2
	v_mul_f32_e32 v2, v67, v36
	v_mul_f32_e32 v3, v67, v37
	v_cvt_pk_bf16_f32 v2, v2, v3
	v_mul_f32_e32 v3, v67, v38
	v_cvt_pk_bf16_f32 v3, v3, v4
	v_permlane32_swap_b32_e32 v0, v2
	s_nop 0
	v_permlane32_swap_b32_e32 v1, v3
	global_store_dwordx4 v[64:65], v[0:3], off offset:128 sc1
	v_mul_f32_e32 v4, v67, v47
	s_add_i32 s3, s2, s94
	v_mul_f32_e32 v0, v67, v40
	v_mul_f32_e32 v1, v67, v41
	v_cvt_pk_bf16_f32 v0, v0, v1
	v_mul_f32_e32 v1, v67, v42
	v_mul_f32_e32 v2, v67, v43
	v_cvt_pk_bf16_f32 v1, v1, v2
	v_mul_f32_e32 v2, v67, v44
	v_mul_f32_e32 v3, v67, v45
	v_cvt_pk_bf16_f32 v2, v2, v3
	v_mul_f32_e32 v3, v67, v46
	v_cvt_pk_bf16_f32 v3, v3, v4
	v_permlane32_swap_b32_e32 v0, v2
	s_nop 0
	v_permlane32_swap_b32_e32 v1, v3
	global_store_dwordx4 v[64:65], v[0:3], off offset:160 sc1
	v_mul_f32_e32 v4, v67, v23
	s_cmp_lt_i32 s3, s37
	v_mul_f32_e32 v0, v67, v16
	v_mul_f32_e32 v1, v67, v17
	v_cvt_pk_bf16_f32 v0, v0, v1
	v_mul_f32_e32 v1, v67, v18
	v_mul_f32_e32 v2, v67, v19
	v_cvt_pk_bf16_f32 v1, v1, v2
	v_mul_f32_e32 v2, v67, v20
	v_mul_f32_e32 v3, v67, v21
	v_cvt_pk_bf16_f32 v2, v2, v3
	v_mul_f32_e32 v3, v67, v22
	v_cvt_pk_bf16_f32 v3, v3, v4
	v_permlane32_swap_b32_e32 v0, v2
	s_nop 0
	v_permlane32_swap_b32_e32 v1, v3
	global_store_dwordx4 v[64:65], v[0:3], off offset:192 sc1
	v_mul_f32_e32 v4, v67, v31
	s_movk_i32 s33, 0xffef
	v_mul_f32_e32 v0, v67, v24
	v_mul_f32_e32 v1, v67, v25
	v_cvt_pk_bf16_f32 v0, v0, v1
	v_mul_f32_e32 v1, v67, v26
	v_mul_f32_e32 v2, v67, v27
	v_cvt_pk_bf16_f32 v1, v1, v2
	v_mul_f32_e32 v2, v67, v28
	v_mul_f32_e32 v3, v67, v29
	v_cvt_pk_bf16_f32 v2, v2, v3
	v_mul_f32_e32 v3, v67, v30
	v_cvt_pk_bf16_f32 v3, v3, v4
	v_permlane32_swap_b32_e32 v0, v2
	s_nop 0
	v_permlane32_swap_b32_e32 v1, v3
	global_store_dwordx4 v[64:65], v[0:3], off offset:224 sc1
	s_cbranch_scc0 .LBB0_889
